# P8 final output rows stored nt (never re-read), on top of combo5
# baseline (speedup 1.0000x reference)
; #define GAS __attribute__((address_space(1)))
; __device__ __forceinline__ float bflo(unsigned w) { return __uint_as_float(w << 16); }
; __device__ __forceinline__ float bfhi(unsigned w) { return __uint_as_float(w & 0xffff0000u); }
; __device__ __forceinline__ void peer_block(LAS unsigned char* wl, int tok0, const unsigned char* XQ, const float* XS, const unsigned char* U8, const unsigned char* V8, const float* SU, const float* SV, const int* IDX, const float* GATE, const bf16* HB, float* HO, bf16* X2, const float* wfin, int lan ...
;     ...
;     for (int j = 0; j < 8; ++j) { const size_t ro = (size_t)(tok0 + j) * D;
;         const GAS u32x2* sp = (const GAS u32x2*)(X2 + ro) + lane; const GAS u32x2* hp = (const GAS u32x2*)(HB + ro) + lane;
;         f32x4 xv[16]; float ss = 0.f;
; #pragma unroll
;         for (int q = 0; q < 16; ++q) { const u32x2 v = sp[64 * q], hv = __builtin_nontemporal_load(hp + 64 * q);
;             xv[q] = (f32x4){bflo(v.x) + bflo(hv.x), bfhi(v.x) + bfhi(hv.x), bflo(v.y) + bflo(hv.y), bfhi(v.y) + bfhi(hv.y)}; ss += (xv[q].x * xv[q].x + xv[q].y * xv[q].y) + (xv[q].z * xv[q].z + xv[q].w * xv[q].w); }
.LBB0_842:
	v_add_co_u32_e32 v70, vcc, s47, v64
	v_lshl_add_u64 v[68:69], v[66:67], 0, s[30:31]
	s_nop 0
	v_addc_co_u32_e32 v71, vcc, 0, v65, vcc
	v_add_co_u32_e32 v72, vcc, s48, v64
	v_add_co_u32_e64 v80, s[2:3], s50, v68
	s_nop 0
	v_addc_co_u32_e32 v73, vcc, 0, v65, vcc
	v_add_co_u32_e32 v74, vcc, s49, v64
	v_addc_co_u32_e64 v81, s[2:3], 0, v69, s[2:3]
	s_nop 0
	v_addc_co_u32_e32 v75, vcc, 0, v65, vcc
	v_add_co_u32_e32 v78, vcc, 0x18300000, v68
	v_add_co_u32_e64 v82, s[2:3], s51, v68
	s_nop 0
	v_addc_co_u32_e32 v79, vcc, 0, v69, vcc
	v_addc_co_u32_e64 v83, s[2:3], 0, v69, s[2:3]
	global_load_dwordx2 v[84:85], v[82:83], off nt
	global_load_dwordx2 v[86:87], v[80:81], off
	global_load_dwordx2 v[88:89], v[80:81], off offset:512
	global_load_dwordx2 v[90:91], v[82:83], off offset:512 nt
	global_load_dwordx2 v[92:93], v[80:81], off offset:1024
	global_load_dwordx2 v[76:77], v[82:83], off offset:1024 nt
	global_load_dwordx2 v[94:95], v[80:81], off offset:1536
	global_load_dwordx2 v[96:97], v[82:83], off offset:1536 nt
	global_load_dwordx2 v[98:99], v[80:81], off offset:2048
	global_load_dwordx2 v[100:101], v[82:83], off offset:2048 nt
	global_load_dwordx2 v[102:103], v[82:83], off offset:2560 nt
	global_load_dwordx2 v[104:105], v[80:81], off offset:2560
	global_load_dwordx2 v[106:107], v[80:81], off offset:3072
	global_load_dwordx2 v[108:109], v[82:83], off offset:3072 nt
	s_nop 0
	global_load_dwordx2 v[80:81], v[80:81], off offset:3584
	v_add_co_u32_e32 v68, vcc, 0x40300000, v68
	global_load_dwordx2 v[110:111], v[82:83], off offset:3584 nt
	s_nop 0
	v_addc_co_u32_e32 v69, vcc, 0, v69, vcc
	global_load_dwordx2 v[82:83], v[78:79], off offset:512
	global_load_dwordx2 v[112:113], v[78:79], off
	global_load_dwordx2 v[114:115], v[78:79], off offset:1024
	global_load_dwordx2 v[116:117], v[78:79], off offset:1536
	global_load_dwordx2 v[118:119], v[78:79], off offset:2048
	global_load_dwordx2 v[120:121], v[78:79], off offset:2560
	global_load_dwordx2 v[122:123], v[78:79], off offset:3072
	s_nop 0
	global_load_dwordx2 v[78:79], v[78:79], off offset:3584
	s_nop 0
	global_load_dwordx2 v[124:125], v[68:69], off nt
	global_load_dwordx2 v[126:127], v[68:69], off offset:512 nt
	global_load_dwordx2 v[128:129], v[68:69], off offset:1024 nt
	global_load_dwordx2 v[130:131], v[68:69], off offset:1536 nt
	global_load_dwordx2 v[132:133], v[68:69], off offset:2048 nt
	global_load_dwordx2 v[134:135], v[68:69], off offset:2560 nt
	global_load_dwordx2 v[156:157], v[68:69], off offset:3072 nt
	global_load_dwordx2 v[186:187], v[68:69], off offset:3584 nt
	s_add_u32 s30, s30, 0x2000
	s_addc_u32 s31, s31, 0
	s_cmp_lg_u32 s30, 0x10000
	s_waitcnt vmcnt(31)
	v_lshlrev_b32_e32 v188, 16, v84
	v_and_b32_e32 v189, 0xffff0000, v84
	v_lshlrev_b32_e32 v192, 16, v85
	v_and_b32_e32 v193, 0xffff0000, v85
	s_waitcnt vmcnt(29)
	v_lshlrev_b32_e32 v68, 16, v88
	v_and_b32_e32 v69, 0xffff0000, v88
	s_waitcnt vmcnt(28)
	v_lshlrev_b32_e32 v84, 16, v90
	v_and_b32_e32 v85, 0xffff0000, v90
	s_waitcnt vmcnt(27)
	v_lshlrev_b32_e32 v139, 16, v92
	v_and_b32_e32 v197, 0xffff0000, v92
	s_waitcnt vmcnt(26)
	v_lshlrev_b32_e32 v200, 16, v77
	v_lshlrev_b32_e32 v92, 16, v93
	v_and_b32_e32 v201, 0xffff0000, v77
	v_and_b32_e32 v93, 0xffff0000, v93
	s_waitcnt vmcnt(25)
	v_lshlrev_b32_e32 v203, 16, v95
	v_lshlrev_b32_e32 v202, 16, v94
	s_waitcnt vmcnt(24)
	v_lshlrev_b32_e32 v205, 16, v97
	v_lshlrev_b32_e32 v204, 16, v96
	v_and_b32_e32 v95, 0xffff0000, v95
	v_and_b32_e32 v94, 0xffff0000, v94
	v_and_b32_e32 v97, 0xffff0000, v97
	v_and_b32_e32 v96, 0xffff0000, v96
	s_waitcnt vmcnt(23)
	v_lshlrev_b32_e32 v206, 16, v98
	v_and_b32_e32 v207, 0xffff0000, v98
	s_waitcnt vmcnt(22)
	v_lshlrev_b32_e32 v208, 16, v100
	v_and_b32_e32 v209, 0xffff0000, v100
	v_lshlrev_b32_e32 v98, 16, v99
	v_and_b32_e32 v99, 0xffff0000, v99
	v_lshlrev_b32_e32 v100, 16, v101
	v_and_b32_e32 v101, 0xffff0000, v101
	v_lshlrev_b32_e32 v190, 16, v86
	v_and_b32_e32 v191, 0xffff0000, v86
	v_lshlrev_b32_e32 v194, 16, v87
	v_and_b32_e32 v195, 0xffff0000, v87
	v_lshlrev_b32_e32 v88, 16, v89
	v_and_b32_e32 v89, 0xffff0000, v89
	v_lshlrev_b32_e32 v90, 16, v91
	v_and_b32_e32 v91, 0xffff0000, v91
	s_waitcnt vmcnt(21)
	v_lshlrev_b32_e32 v210, 16, v102
	s_waitcnt vmcnt(20)
	v_lshlrev_b32_e32 v212, 16, v104
	v_and_b32_e32 v211, 0xffff0000, v102
	v_and_b32_e32 v213, 0xffff0000, v104
	s_waitcnt vmcnt(19)
	v_lshlrev_b32_e32 v214, 16, v106
	v_and_b32_e32 v215, 0xffff0000, v106
	s_waitcnt vmcnt(18)
	v_lshlrev_b32_e32 v216, 16, v108
	v_and_b32_e32 v217, 0xffff0000, v108
	v_lshlrev_b32_e32 v106, 16, v107
	v_and_b32_e32 v107, 0xffff0000, v107
	v_lshlrev_b32_e32 v108, 16, v109
	v_and_b32_e32 v109, 0xffff0000, v109
	s_waitcnt vmcnt(17)
	v_lshlrev_b32_e32 v155, 16, v80
	v_and_b32_e32 v219, 0xffff0000, v80
	v_lshlrev_b32_e32 v224, 16, v81
	v_and_b32_e32 v225, 0xffff0000, v81
	s_waitcnt vmcnt(15)
	v_lshlrev_b32_e32 v227, 16, v83
	v_lshlrev_b32_e32 v226, 16, v82
	v_and_b32_e32 v229, 0xffff0000, v83
	v_and_b32_e32 v228, 0xffff0000, v82
	s_waitcnt vmcnt(9)
	v_lshlrev_b32_e32 v237, 16, v123
	v_lshlrev_b32_e32 v236, 16, v122
	v_and_b32_e32 v123, 0xffff0000, v123
	v_and_b32_e32 v122, 0xffff0000, v122
	v_pk_add_f32 v[86:87], v[68:69], v[84:85]
	v_pk_add_f32 v[84:85], v[94:95], v[96:97]
	v_pk_add_f32 v[80:81], v[206:207], v[208:209]
	v_pk_add_f32 v[82:83], v[98:99], v[100:101]
	v_lshlrev_b32_e32 v94, 16, v112
	v_and_b32_e32 v95, 0xffff0000, v112
	v_lshlrev_b32_e32 v96, 16, v113
	v_and_b32_e32 v97, 0xffff0000, v113
	v_pk_add_f32 v[92:93], v[92:93], v[200:201]
	s_waitcnt vmcnt(6)
	v_and_b32_e32 v113, 0xffff0000, v127
	v_and_b32_e32 v112, 0xffff0000, v126
	s_waitcnt vmcnt(1)
; __device__ __forceinline__ float bflo(unsigned w) { return __uint_as_float(w << 16); }
; __device__ __forceinline__ float bfhi(unsigned w) { return __uint_as_float(w & 0xffff0000u); }
; __device__ __forceinline__ void peer_block(LAS unsigned char* wl, int tok0, const unsigned char* XQ, const float* XS, const unsigned char* U8, const unsigned char* V8, const float* SU, const float* SV, const int* IDX, const float* GATE, const bf16* HB, float* HO, bf16* X2, const float* wfin, int lan ...
;     ...
;         for (int q = 0; q < 16; ++q) { const u32x2 v = sp[64 * q], hv = __builtin_nontemporal_load(hp + 64 * q);
;             xv[q] = (f32x4){bflo(v.x) + bflo(hv.x), bfhi(v.x) + bfhi(hv.x), bflo(v.y) + bflo(hv.y), bfhi(v.y) + bfhi(hv.y)}; ss += (xv[q].x * xv[q].x + xv[q].y * xv[q].y) + (xv[q].z * xv[q].z + xv[q].w * xv[q].w); }
	v_lshlrev_b32_e32 v201, 16, v157
	v_lshlrev_b32_e32 v200, 16, v156
	v_and_b32_e32 v157, 0xffff0000, v157
	v_and_b32_e32 v156, 0xffff0000, v156
	v_lshlrev_b32_e32 v206, 16, v124
	v_and_b32_e32 v207, 0xffff0000, v124
	v_lshlrev_b32_e32 v124, 16, v125
	v_and_b32_e32 v125, 0xffff0000, v125
	v_lshlrev_b32_e32 v102, 16, v103
	v_lshlrev_b32_e32 v104, 16, v105
	v_and_b32_e32 v103, 0xffff0000, v103
	v_and_b32_e32 v105, 0xffff0000, v105
	v_lshlrev_b32_e32 v222, 16, v111
	v_and_b32_e32 v223, 0xffff0000, v111
	v_lshlrev_b32_e32 v232, 16, v116
	v_and_b32_e32 v233, 0xffff0000, v116
	v_lshlrev_b32_e32 v116, 16, v117
	v_and_b32_e32 v117, 0xffff0000, v117
	v_lshlrev_b32_e32 v234, 16, v118
	v_and_b32_e32 v235, 0xffff0000, v118
	v_lshlrev_b32_e32 v118, 16, v119
	v_and_b32_e32 v119, 0xffff0000, v119
	v_lshlrev_b32_e32 v246, 16, v120
	v_and_b32_e32 v111, 0xffff0000, v120
	v_lshlrev_b32_e32 v120, 16, v121
	v_and_b32_e32 v121, 0xffff0000, v121
	v_lshlrev_b32_e32 v238, 16, v78
	v_and_b32_e32 v239, 0xffff0000, v78
	v_lshlrev_b32_e32 v240, 16, v79
	v_and_b32_e32 v241, 0xffff0000, v79
	v_pk_add_f32 v[88:89], v[88:89], v[90:91]
	v_pk_add_f32 v[90:91], v[202:203], v[204:205]
	v_pk_add_f32 v[68:69], v[214:215], v[216:217]
	v_pk_add_f32 v[78:79], v[106:107], v[108:109]
	v_pk_add_f32 v[98:99], v[190:191], v[188:189]
	v_pk_add_f32 v[100:101], v[194:195], v[192:193]
	v_pk_add_f32 v[106:107], v[212:213], v[210:211]
	v_lshlrev_b32_e32 v109, 16, v127
	v_lshlrev_b32_e32 v108, 16, v126
	v_lshlrev_b32_e32 v188, 16, v130
	v_and_b32_e32 v189, 0xffff0000, v130
	v_lshlrev_b32_e32 v130, 16, v131
	v_and_b32_e32 v131, 0xffff0000, v131
	v_lshlrev_b32_e32 v190, 16, v132
	v_and_b32_e32 v191, 0xffff0000, v132
	v_lshlrev_b32_e32 v132, 16, v133
	v_and_b32_e32 v133, 0xffff0000, v133
	v_lshlrev_b32_e32 v194, 16, v135
	v_and_b32_e32 v195, 0xffff0000, v135
	v_pk_mul_f32 v[204:205], v[84:85], v[84:85]
	v_mul_f32_e32 v210, v83, v83
	v_pk_add_f32 v[112:113], v[228:229], v[112:113]
	v_pk_add_f32 v[122:123], v[122:123], v[156:157]
	v_pk_add_f32 v[94:95], v[94:95], v[206:207]
	v_pk_add_f32 v[96:97], v[96:97], v[124:125]
	v_and_b32_e32 v199, 0xffff0000, v76
	v_lshlrev_b32_e32 v230, 16, v114
	v_and_b32_e32 v231, 0xffff0000, v114
	v_lshlrev_b32_e32 v114, 16, v115
	v_and_b32_e32 v115, 0xffff0000, v115
	v_pk_add_f32 v[102:103], v[104:105], v[102:103]
	v_pk_add_f32 v[104:105], v[224:225], v[222:223]
	v_lshlrev_b32_e32 v126, 16, v128
	v_and_b32_e32 v127, 0xffff0000, v128
	v_lshlrev_b32_e32 v128, 16, v129
	v_and_b32_e32 v129, 0xffff0000, v129
	v_and_b32_e32 v193, 0xffff0000, v134
	s_waitcnt vmcnt(0)
	v_lshlrev_b32_e32 v202, 16, v186
	v_and_b32_e32 v203, 0xffff0000, v186
	v_mul_f32_e32 v140, v87, v87
	v_mul_f32_e32 v192, v89, v89
	v_mul_f32_e32 v196, v69, v69
	v_mul_f32_e32 v198, v79, v79
	v_mul_f32_e32 v208, v81, v81
	v_mov_b32_e32 v222, v90
	v_mov_b32_e32 v223, v84
	v_mov_b32_e32 v84, v91
	v_pk_add_f32 v[108:109], v[226:227], v[108:109]
	v_pk_add_f32 v[118:119], v[118:119], v[132:133]
	v_pk_add_f32 v[132:133], v[236:237], v[200:201]
	v_pk_fma_f32 v[90:91], v[90:91], v[90:91], v[204:205]
	v_pk_fma_f32 v[206:207], v[82:83], v[82:83], v[210:211] op_sel_hi:[1,1,0]
	v_pk_add_f32 v[188:189], v[232:233], v[188:189]
	v_pk_add_f32 v[116:117], v[116:117], v[130:131]
	v_pk_add_f32 v[120:121], v[120:121], v[194:195]
	v_pk_mul_f32 v[130:131], v[112:113], v[112:113]
	v_pk_mul_f32 v[194:195], v[122:123], v[122:123]
	v_mov_b32_e32 v210, v95
	v_mov_b32_e32 v211, v97
	v_pk_mul_f32 v[212:213], v[98:99], v[98:99]
	v_pk_mul_f32 v[216:217], v[92:93], v[92:93]
	v_pk_mul_f32 v[224:225], v[106:107], v[106:107]
	v_pk_mul_f32 v[244:245], v[104:105], v[104:105]
	v_pk_add_f32 v[126:127], v[230:231], v[126:127]
	v_pk_add_f32 v[114:115], v[114:115], v[128:129]
	v_pk_add_f32 v[128:129], v[234:235], v[190:191]
	v_pk_add_f32 v[156:157], v[238:239], v[202:203]
	v_pk_fma_f32 v[190:191], v[86:87], v[86:87], v[140:141] op_sel_hi:[1,1,0]
	v_pk_fma_f32 v[200:201], v[88:89], v[88:89], v[192:193] op_sel_hi:[1,1,0]
	v_pk_fma_f32 v[202:203], v[68:69], v[68:69], v[196:197] op_sel_hi:[1,1,0]
	v_pk_fma_f32 v[204:205], v[78:79], v[78:79], v[198:199] op_sel_hi:[1,1,0]
	v_pk_fma_f32 v[124:125], v[80:81], v[80:81], v[208:209] op_sel_hi:[1,1,0]
	v_mul_f32_e32 v192, v119, v119
	v_pk_add_f32 v[90:91], v[90:91], v[90:91] op_sel:[0,1] op_sel_hi:[1,0]
	v_mov_b32_e32 v208, v94
	v_mov_b32_e32 v209, v96
	v_mov_b32_e32 v230, v108
	v_mov_b32_e32 v231, v112
	v_mov_b32_e32 v112, v109
	v_pk_mul_f32 v[232:233], v[188:189], v[188:189]
	v_mov_b32_e32 v238, v132
	v_mov_b32_e32 v239, v122
	v_mov_b32_e32 v122, v133
	v_pk_fma_f32 v[108:109], v[108:109], v[108:109], v[130:131]
	v_pk_fma_f32 v[132:133], v[132:133], v[132:133], v[194:195]
	v_pk_mul_f32 v[194:195], v[210:211], v[210:211]
	v_and_b32_e32 v221, 0xffff0000, v110
	v_mov_b32_e32 v196, v212
	v_mov_b32_e32 v218, v224
	v_mul_f32_e32 v212, v127, v127
	v_mul_f32_e32 v224, v115, v115
	v_pk_mul_f32 v[234:235], v[116:117], v[116:117]
	v_mov_b32_e32 v191, v216
	v_mov_b32_e32 v201, v217
	v_mov_b32_e32 v203, v244
	v_mov_b32_e32 v205, v245
	v_pk_fma_f32 v[216:217], v[118:119], v[118:119], v[192:193] op_sel_hi:[1,1,0]
	v_lshlrev_b32_e32 v91, 16, v110
	v_mov_b32_e32 v110, v232
	v_mov_b32_e32 v192, v233
	v_pk_add_f32 v[108:109], v[108:109], v[108:109] op_sel:[0,1] op_sel_hi:[1,0]
	v_pk_add_f32 v[132:133], v[132:133], v[132:133] op_sel:[0,1] op_sel_hi:[1,0]
	v_pk_fma_f32 v[194:195], v[208:209], v[208:209], v[194:195]
	v_mov_b32_e32 v198, v213
	v_pk_fma_f32 v[210:211], v[126:127], v[126:127], v[212:213] op_sel_hi:[1,1,0]
	v_pk_fma_f32 v[212:213], v[114:115], v[114:115], v[224:225] op_sel_hi:[1,1,0]
	v_pk_add_f32 v[190:191], v[190:191], v[200:201]
; __device__ __forceinline__ float bflo(unsigned w) { return __uint_as_float(w << 16); }
; __device__ __forceinline__ float bfhi(unsigned w) { return __uint_as_float(w & 0xffff0000u); }
; __device__ __forceinline__ void peer_block(LAS unsigned char* wl, int tok0, const unsigned char* XQ, const float* XS, const unsigned char* U8, const unsigned char* V8, const float* SU, const float* SV, const int* IDX, const float* GATE, const bf16* HB, float* HO, bf16* X2, const float* wfin, int lan ...
;     ...
;             xv[q] = (f32x4){bflo(v.x) + bflo(hv.x), bfhi(v.x) + bfhi(hv.x), bflo(v.y) + bflo(hv.y), bfhi(v.y) + bfhi(hv.y)}; ss += (xv[q].x * xv[q].x + xv[q].y * xv[q].y) + (xv[q].z * xv[q].z + xv[q].w * xv[q].w); }
;         const float rs = 1.0f / sqrtf(wave_sum(ss) * (1.f / D) + EPS);
	v_pk_add_f32 v[200:201], v[202:203], v[204:205]
	v_pk_add_f32 v[202:203], v[110:111], v[192:193]
	v_mov_b32_e32 v110, v234
	v_mov_b32_e32 v192, v235
	v_lshlrev_b32_e32 v109, 16, v134
	v_lshlrev_b32_e32 v133, 16, v76
	v_pk_add_f32 v[76:77], v[194:195], v[194:195] op_sel:[0,1] op_sel_hi:[1,0]
	v_mov_b32_e32 v211, v246
	v_pk_add_f32 v[110:111], v[110:111], v[192:193]
	v_mov_b32_e32 v213, v109
	v_mov_b32_e32 v77, v246
	v_mul_f32_e32 v140, v129, v129
	v_pk_add_f32 v[134:135], v[202:203], v[110:111]
	v_pk_mul_f32 v[110:111], v[202:203], v[110:111]
	v_pk_add_f32 v[192:193], v[210:211], v[212:213]
	v_pk_add_f32 v[76:77], v[76:77], v[108:109]
	v_pk_mul_f32 v[236:237], v[120:121], v[120:121]
	v_pk_fma_f32 v[130:131], v[128:129], v[128:129], v[140:141] op_sel_hi:[1,1,0]
	v_mov_b32_e32 v135, v111
	v_pk_add_f32 v[110:111], v[76:77], v[192:193]
	v_pk_mul_f32 v[192:193], v[76:77], v[192:193]
	v_lshlrev_b32_e32 v186, 16, v187
	v_and_b32_e32 v187, 0xffff0000, v187
	v_mov_b32_e32 v131, v236
	v_mov_b32_e32 v217, v237
	v_mov_b32_e32 v111, v193
	v_pk_add_f32 v[186:187], v[240:241], v[186:187]
	v_pk_add_f32 v[130:131], v[130:131], v[216:217]
	v_mov_b32_e32 v202, v77
	v_pk_add_f32 v[76:77], v[110:111], v[134:135]
	v_mul_f32_e32 v226, v157, v157
	v_mul_f32_e32 v228, v187, v187
	v_pk_add_f32 v[76:77], v[76:77], v[130:131]
	v_pk_mul_f32 v[214:215], v[100:101], v[100:101]
	v_mov_b32_e32 v220, v225
	v_pk_fma_f32 v[224:225], v[156:157], v[156:157], v[226:227] op_sel_hi:[1,1,0]
	v_pk_fma_f32 v[226:227], v[186:187], v[186:187], v[228:229] op_sel_hi:[1,1,0]
	v_pk_add_f32 v[76:77], v[76:77], v[76:77] op_sel:[0,1] op_sel_hi:[1,0]
	v_pk_add_f32 v[240:241], v[196:197], v[198:199]
	v_mov_b32_e32 v196, v214
	v_mov_b32_e32 v198, v215
	v_mov_b32_e32 v225, v139
	v_mov_b32_e32 v227, v133
	v_mov_b32_e32 v77, v139
	v_pk_add_f32 v[196:197], v[196:197], v[198:199]
	v_pk_add_f32 v[108:109], v[224:225], v[226:227]
	v_pk_add_f32 v[76:77], v[76:77], v[132:133]
	v_pk_add_f32 v[204:205], v[240:241], v[196:197]
	v_pk_mul_f32 v[196:197], v[240:241], v[196:197]
	v_pk_add_f32 v[110:111], v[76:77], v[108:109]
	v_pk_mul_f32 v[108:109], v[76:77], v[108:109]
	v_mov_b32_e32 v205, v197
	v_mov_b32_e32 v111, v109
	v_mov_b32_e32 v240, v77
	v_pk_add_f32 v[76:77], v[110:111], v[204:205]
	v_pk_mul_f32 v[242:243], v[102:103], v[102:103]
	v_pk_add_f32 v[76:77], v[76:77], v[190:191]
	v_mov_b32_e32 v125, v155
	v_pk_add_f32 v[76:77], v[76:77], v[76:77] op_sel:[0,1] op_sel_hi:[1,0]
	v_pk_add_f32 v[214:215], v[218:219], v[220:221]
	v_mov_b32_e32 v218, v242
	v_mov_b32_e32 v220, v243
	v_mov_b32_e32 v207, v91
	v_mov_b32_e32 v77, v155
	v_pk_add_f32 v[198:199], v[218:219], v[220:221]
	v_pk_add_f32 v[124:125], v[124:125], v[206:207]
	v_pk_add_f32 v[76:77], v[76:77], v[90:91]
	v_pk_add_f32 v[208:209], v[214:215], v[198:199]
	v_pk_mul_f32 v[198:199], v[214:215], v[198:199]
	v_pk_add_f32 v[90:91], v[76:77], v[124:125]
	v_pk_mul_f32 v[108:109], v[76:77], v[124:125]
	v_mov_b32_e32 v209, v199
	v_mov_b32_e32 v91, v109
	v_mov_b32_e32 v214, v77
	v_pk_add_f32 v[76:77], v[90:91], v[208:209]
	s_nop 0
	v_pk_add_f32 v[76:77], v[76:77], v[200:201]
	s_nop 0
	v_add_f32_e32 v76, v76, v77
	ds_bpermute_b32 v77, v181, v76
	s_waitcnt lgkmcnt(0)
	v_add_f32_e32 v76, v76, v77
	ds_bpermute_b32 v77, v180, v76
	s_waitcnt lgkmcnt(0)
	v_add_f32_e32 v76, v76, v77
	ds_bpermute_b32 v77, v179, v76
	s_waitcnt lgkmcnt(0)
	v_add_f32_e32 v76, v76, v77
	ds_bpermute_b32 v77, v136, v76
	s_waitcnt lgkmcnt(0)
	v_add_f32_e32 v76, v76, v77
	ds_bpermute_b32 v77, v138, v76
	s_waitcnt lgkmcnt(0)
	v_add_f32_e32 v76, v76, v77
	ds_bpermute_b32 v77, v137, v76
	s_waitcnt lgkmcnt(0)
; #define GAS __attribute__((address_space(1)))
; __device__ __forceinline__ void peer_block(LAS unsigned char* wl, int tok0, const unsigned char* XQ, const float* XS, const unsigned char* U8, const unsigned char* V8, const float* SU, const float* SV, const int* IDX, const float* GATE, const bf16* HB, float* HO, bf16* X2, const float* wfin, int lan ...
;     ...
;         const float rs = 1.0f / sqrtf(wave_sum(ss) * (1.f / D) + EPS);
;         GAS f32x4* rp = (GAS f32x4*)(HO + ro) + lane;
; #pragma unroll
;         for (int q = 0; q < 16; ++q) { const f32x4 g = gfin[q]; rp[64 * q] = (f32x4){xv[q].x * rs * g.x, xv[q].y * rs * g.y, xv[q].z * rs * g.z, xv[q].w * rs * g.w}; } }
	v_add_f32_e32 v76, v76, v77
	v_fmamk_f32 v76, v76, 0x39800000, v169
	v_mul_f32_e32 v77, 0x4f800000, v76
	v_cmp_gt_f32_e32 vcc, s52, v76
	s_nop 1
	v_cndmask_b32_e32 v76, v76, v77, vcc
	v_sqrt_f32_e32 v77, v76
	s_nop 0
	v_add_u32_e32 v90, -1, v77
	v_add_u32_e32 v91, 1, v77
	v_fma_f32 v108, -v90, v77, v76
	v_fma_f32 v109, -v91, v77, v76
	v_cmp_ge_f32_e64 s[2:3], 0, v108
	s_nop 1
	v_cndmask_b32_e64 v77, v77, v90, s[2:3]
	v_cmp_lt_f32_e64 s[2:3], 0, v109
	s_nop 1
	v_cndmask_b32_e64 v77, v77, v91, s[2:3]
	v_mul_f32_e32 v90, 0x37800000, v77
	v_cndmask_b32_e32 v77, v77, v90, vcc
	v_cmp_class_f32_e32 vcc, v76, v170
	s_nop 1
	v_cndmask_b32_e32 v76, v77, v76, vcc
	v_div_scale_f32 v77, s[2:3], v76, v76, 1.0
	v_rcp_f32_e32 v91, v77
	v_div_scale_f32 v90, vcc, 1.0, v76, 1.0
	v_fma_f32 v108, -v77, v91, 1.0
	v_fmac_f32_e32 v91, v108, v91
	v_mul_f32_e32 v108, v90, v91
	v_fma_f32 v109, -v77, v108, v90
	v_fmac_f32_e32 v108, v109, v91
	v_fma_f32 v77, -v77, v108, v90
	v_div_fmas_f32 v77, v77, v91, v108
	v_div_fixup_f32 v76, v77, v76, 1.0
	v_pk_mul_f32 v[90:91], v[94:95], v[76:77] op_sel_hi:[1,0]
	v_pk_mul_f32 v[94:95], v[96:97], v[76:77] op_sel_hi:[1,0]
	v_pk_mul_f32 v[96:97], v[230:231], v[76:77] op_sel_hi:[1,0]
	v_pk_mul_f32 v[108:109], v[112:113], v[76:77] op_sel_hi:[1,0]
	v_pk_mul_f32 v[110:111], v[126:127], v[76:77] op_sel_hi:[1,0]
	v_pk_mul_f32 v[112:113], v[114:115], v[76:77] op_sel_hi:[1,0]
	v_pk_mul_f32 v[114:115], v[188:189], v[76:77] op_sel_hi:[1,0]
	v_pk_mul_f32 v[116:117], v[116:117], v[76:77] op_sel_hi:[1,0]
	v_pk_mul_f32 v[124:125], v[128:129], v[76:77] op_sel_hi:[1,0]
	v_pk_mul_f32 v[118:119], v[118:119], v[76:77] op_sel_hi:[1,0]
	v_pk_mul_f32 v[126:127], v[202:203], v[76:77] op_sel_hi:[1,0]
	v_pk_mul_f32 v[120:121], v[120:121], v[76:77] op_sel_hi:[1,0]
	v_pk_mul_f32 v[128:129], v[238:239], v[76:77] op_sel_hi:[1,0]
	v_pk_mul_f32 v[122:123], v[122:123], v[76:77] op_sel_hi:[1,0]
	v_pk_mul_f32 v[130:131], v[156:157], v[76:77] op_sel_hi:[1,0]
	v_pk_mul_f32 v[132:133], v[186:187], v[76:77] op_sel_hi:[1,0]
	v_pk_mul_f32 v[134:135], v[98:99], v[76:77] op_sel_hi:[1,0]
	v_pk_mul_f32 v[156:157], v[100:101], v[76:77] op_sel_hi:[1,0]
	v_pk_mul_f32 v[186:187], v[86:87], v[76:77] op_sel_hi:[1,0]
	v_pk_mul_f32 v[188:189], v[88:89], v[76:77] op_sel_hi:[1,0]
	v_pk_mul_f32 v[190:191], v[240:241], v[76:77] op_sel_hi:[1,0]
	v_pk_mul_f32 v[192:193], v[92:93], v[76:77] op_sel_hi:[1,0]
	v_pk_mul_f32 v[194:195], v[222:223], v[76:77] op_sel_hi:[1,0]
	v_pk_mul_f32 v[196:197], v[84:85], v[76:77] op_sel_hi:[1,0]
	v_pk_mul_f32 v[198:199], v[80:81], v[76:77] op_sel_hi:[1,0]
	v_pk_mul_f32 v[200:201], v[82:83], v[76:77] op_sel_hi:[1,0]
	v_pk_mul_f32 v[202:203], v[106:107], v[76:77] op_sel_hi:[1,0]
	v_pk_mul_f32 v[204:205], v[102:103], v[76:77] op_sel_hi:[1,0]
	v_pk_mul_f32 v[68:69], v[68:69], v[76:77] op_sel_hi:[1,0]
	v_pk_mul_f32 v[206:207], v[78:79], v[76:77] op_sel_hi:[1,0]
	v_pk_mul_f32 v[208:209], v[214:215], v[76:77] op_sel_hi:[1,0]
	v_pk_mul_f32 v[210:211], v[104:105], v[76:77] op_sel_hi:[1,0]
	v_pk_mul_f32 v[78:79], v[2:3], v[94:95]
	v_pk_mul_f32 v[76:77], v[0:1], v[90:91]
	v_pk_mul_f32 v[80:81], v[4:5], v[96:97]
	v_pk_mul_f32 v[82:83], v[6:7], v[108:109]
	v_pk_mul_f32 v[86:87], v[10:11], v[112:113]
	v_pk_mul_f32 v[84:85], v[8:9], v[110:111]
	v_pk_mul_f32 v[90:91], v[14:15], v[116:117]
	v_pk_mul_f32 v[88:89], v[12:13], v[114:115]
	v_pk_mul_f32 v[94:95], v[18:19], v[118:119]
	v_pk_mul_f32 v[92:93], v[16:17], v[124:125]
	v_pk_mul_f32 v[96:97], v[20:21], v[126:127]
	v_pk_mul_f32 v[98:99], v[22:23], v[120:121]
	v_pk_mul_f32 v[100:101], v[24:25], v[128:129]
	v_pk_mul_f32 v[102:103], v[26:27], v[122:123]
	v_pk_mul_f32 v[106:107], v[30:31], v[132:133]
	v_pk_mul_f32 v[104:105], v[28:29], v[130:131]
	v_pk_mul_f32 v[110:111], v[34:35], v[156:157]
	v_pk_mul_f32 v[108:109], v[32:33], v[134:135]
	v_pk_mul_f32 v[114:115], v[38:39], v[188:189]
	v_pk_mul_f32 v[112:113], v[36:37], v[186:187]
	v_pk_mul_f32 v[116:117], v[40:41], v[190:191]
	v_pk_mul_f32 v[118:119], v[42:43], v[192:193]
	v_pk_mul_f32 v[120:121], v[44:45], v[194:195]
	v_pk_mul_f32 v[122:123], v[46:47], v[196:197]
	v_pk_mul_f32 v[126:127], v[50:51], v[200:201]
	v_pk_mul_f32 v[124:125], v[48:49], v[198:199]
	v_pk_mul_f32 v[130:131], v[54:55], v[204:205]
	v_pk_mul_f32 v[128:129], v[52:53], v[202:203]
	v_pk_mul_f32 v[134:135], v[58:59], v[206:207]
	v_pk_mul_f32 v[132:133], v[56:57], v[68:69]
	v_pk_mul_f32 v[186:187], v[60:61], v[208:209]
	v_pk_mul_f32 v[188:189], v[62:63], v[210:211]
	global_store_dwordx4 v[64:65], v[76:79], off nt
	global_store_dwordx4 v[64:65], v[80:83], off offset:1024 nt
	global_store_dwordx4 v[64:65], v[84:87], off offset:2048 nt
	global_store_dwordx4 v[64:65], v[88:91], off offset:3072 nt
	global_store_dwordx4 v[72:73], v[92:95], off offset:-4096 nt
	global_store_dwordx4 v[70:71], v[96:99], off offset:1024 nt
	global_store_dwordx4 v[70:71], v[100:103], off offset:2048 nt
	global_store_dwordx4 v[70:71], v[104:107], off offset:3072 nt
	global_store_dwordx4 v[72:73], v[108:111], off nt
	global_store_dwordx4 v[72:73], v[112:115], off offset:1024 nt
	global_store_dwordx4 v[72:73], v[116:119], off offset:2048 nt
	global_store_dwordx4 v[72:73], v[120:123], off offset:3072 nt
	global_store_dwordx4 v[74:75], v[124:127], off nt
	global_store_dwordx4 v[74:75], v[128:131], off offset:1024 nt
	global_store_dwordx4 v[74:75], v[132:135], off offset:2048 nt
	global_store_dwordx4 v[74:75], v[186:189], off offset:3072 nt
	v_lshl_add_u64 v[64:65], v[64:65], 0, s[28:29]
	s_cbranch_scc1 .LBB0_842
	s_add_i32 s33, s33, s60
	s_add_i32 s24, s24, s35
	s_cmpk_lt_i32 s33, 0x800
	s_cbranch_scc1 .LBB0_821
